# same as previous, split re-tuned: 107 converter workgroups so the 149 GEMM workgroups need 19 instead of 20 rounds in the dense gate/up phase
# baseline (speedup 1.0000x reference)
.LBB0_839:
	s_add_u32 s16, s56, 0x3eb00000
	s_addc_u32 s17, s57, 0
	s_cmp_lt_i32 s58, 8
	s_cselect_b64 s[0:1], -1, 0
	s_cmp_gt_i32 s59, 7
	s_cselect_b64 s[2:3], -1, 0
	s_and_b64 s[0:1], s[0:1], s[2:3]
	s_andn2_b64 vcc, exec, s[0:1]
	s_cbranch_vccnz .LBB0_921
	s_mov_b32 s99, s13
	s_cmp_lt_u32 s12, 149
	s_cbranch_scc1 .Lsp7_gemm
	s_mov_b32 s98, s12
	s_add_i32 s12, s12, -85
	s_mov_b32 s13, 107
	v_lshrrev_b32_e32 v140, 3, v0
	s_add_u32 s0, s94, 0xffffffe0
	s_addc_u32 s1, s95, -1
	s_load_dwordx2 s[52:53], s[0:1], 0x0
	s_waitcnt lgkmcnt(0)
	s_branch .Lcv_364
.Lsp7_gemm:
	s_mov_b32 s13, 149
	s_cmpk_gt_i32 s12, 0xaff
	v_readfirstlane_b32 s3, v0
	s_cbranch_scc1 .LBB0_867
	v_lshlrev_b32_e32 v2, 4, v0
	v_and_b32_e32 v3, 32, v0
	v_bitop3_b32 v2, v2, v3, 48 bitop3:0x6c
	v_lshrrev_b32_e32 v3, 1, v0
	v_lshrrev_b32_e32 v5, 5, v0
	v_and_b32_e32 v3, 24, v3
	v_and_b32_e32 v5, 4, v5
	s_waitcnt vmcnt(14)
	v_bfe_u32 v6, v0, 2, 2
	v_bfe_u32 v4, v0, 2, 4
	v_or3_b32 v3, v5, v6, v3
	v_lshrrev_b32_e32 v5, 3, v0
	v_and_or_b32 v2, v0, 64, v2
	v_and_or_b32 v6, v5, 48, v4
	v_and_or_b32 v5, v5, 32, v3
	s_lshr_b32 s6, s3, 6
	v_lshl_or_b32 v202, v5, 11, v2
	v_bfe_u32 v5, v0, 3, 25
	s_lshr_b32 s14, s3, 8
	s_lshl_b32 s10, s6, 10
	v_or_b32_e32 v5, 64, v5
	s_movk_i32 s0, 0x70
	s_add_u32 s11, s56, 0x4db00000
	v_and_or_b32 v4, v5, s0, v4
	s_movk_i32 s0, 0x60
	s_addc_u32 s18, s57, 0
	s_ashr_i32 s19, s12, 31
	v_and_or_b32 v3, v5, s0, v3
	s_lshr_b32 s0, s19, 29
	s_add_i32 s0, s12, s0
	s_ashr_i32 s1, s0, 3
	s_and_b32 s0, s0, -8
	s_sub_i32 s0, s12, s0
	s_cmp_lt_i32 s0, 0
	s_movk_i32 s20, 0x161
	s_cselect_b32 s2, s20, 0x160
	s_mul_i32 s0, s0, s2
	s_add_i32 s0, s0, s1
	s_mul_hi_i32 s1, s0, 0x2e8ba2e9
	s_lshr_b32 s2, s1, 31
	s_ashr_i32 s1, s1, 6
	s_add_i32 s1, s1, s2
	s_lshl_b32 s4, s1, 3
	s_mulk_i32 s1, 0x160
	s_sub_i32 s0, s0, s1
	s_sext_i32_i16 s1, s0
	s_bfe_u32 s1, s1, 0x3001c
	s_add_i32 s1, s0, s1
	s_sext_i32_i16 s2, s1
	s_and_b32 s1, s1, 0xfff8
	s_sub_i32 s0, s0, s1
	s_sext_i32_i16 s0, s0
	s_add_i32 s0, s4, s0
	s_ashr_i32 s1, s0, 31
	s_lshr_b32 s2, s2, 3
	s_lshl_b64 s[4:5], s[0:1], 19
	s_add_u32 s26, s24, s4
	s_addc_u32 s27, s25, s5
	s_bfe_i64 s[4:5], s[2:3], 0x100000
	s_lshl_b64 s[4:5], s[4:5], 19
	s_add_u32 s8, s11, s4
	s_addc_u32 s9, s18, s5
	s_add_i32 s1, s10, 0
	v_lshl_or_b32 v201, v6, 11, v2
	v_lshl_or_b32 v203, v4, 11, v2
	v_lshl_or_b32 v204, v3, 11, v2
	s_mov_b64 s[4:5], s[8:9]
	s_add_i32 s21, s1, 0x10000
	v_mov_b32_e32 v2, v202
	s_mov_b32 m0, s21
	s_add_i32 s33, s1, 0x12000
	global_load_lds_dwordx4 v2, s[4:5]
	v_mov_b32_e32 v2, v204
	s_mov_b32 m0, s33
	s_mov_b32 s7, 0
	global_load_lds_dwordx4 v2, s[4:5]
	s_add_u32 s4, s8, 0x40000
	s_addc_u32 s5, s9, 0
	s_add_i32 s35, s1, 0x14000
	v_mov_b32_e32 v2, v202
	s_mov_b32 m0, s35
	s_add_i32 s60, s1, 0x16000
	global_load_lds_dwordx4 v2, s[4:5]
	v_mov_b32_e32 v2, v204
	s_mov_b32 m0, s60
	s_add_i32 s61, s1, 0x2000
	global_load_lds_dwordx4 v2, s[4:5]
	s_mov_b64 s[4:5], s[26:27]
	v_mov_b32_e32 v2, v201
	s_mov_b32 m0, s1
	s_nop 0
	global_load_lds_dwordx4 v2, s[4:5]
	v_mov_b32_e32 v2, v203
	s_mov_b32 m0, s61
	s_nop 0
	global_load_lds_dwordx4 v2, s[4:5]
	s_add_u32 s4, s26, 0x40000
	s_addc_u32 s5, s27, 0
	s_add_i32 s62, s1, 0x4000
	v_mov_b32_e32 v2, v201
	s_mov_b32 m0, s62
	s_add_i32 s63, s1, 0x6000
	global_load_lds_dwordx4 v2, s[4:5]
	v_mov_b32_e32 v2, v203
	s_mov_b32 m0, s63
	s_cmp_eq_u32 s14, 1
	global_load_lds_dwordx4 v2, s[4:5]
	s_cselect_b64 s[4:5], -1, 0
	s_cmp_lg_u32 s14, 1
	s_cbranch_scc1 .LBB0_843
	s_barrier
